# P10 cooperative prefetch at SP2(0): k-tiles 2,3 of unit u+1 and k-tiles 0,1 of unit u+2
# speedup vs baseline: 1.0060x; 1.0060x over previous
.LBB0_1441:
	s_and_b64 vcc, exec, s[0:1]
	s_cmp_eq_u32 s98, 0
	s_cbranch_scc1 .Lgk_first_p10
	v_mov_b32_e32 v175, v169
	v_mov_b32_e32 v173, v169
	s_mov_b32 s23, 0
	s_mov_b64 s[34:35], 0x100
	s_mov_b64 s[36:37], s[16:17]
	v_readfirstlane_b32 s70, v0
	s_lshr_b32 s70, s70, 6
	s_add_i32 s71, s53, 1
	s_mul_i32 s71, s71, s52
	s_add_i32 s71, s71, s33
	s_lshr_b32 s72, s71, 3
	s_add_i32 s72, s72, s42
	s_cmp_lt_i32 s72, s43
	s_cselect_b32 s72, s72, s66
	v_mov_b32_e32 v249, s72
	v_add_u32_e32 v249, 0x24800, v249
	ds_read_u8 v249, v249
	s_cmp_eq_u64 s[2:3], 0
	s_cselect_b32 s71, s65, s66
	s_and_b32 s75, s70, 1
	s_lshl_b32 s73, s28, 14
	s_cmp_eq_u32 s75, 0
	s_cselect_b32 s74, s71, s72
	s_cselect_b32 s76, 0x100, 0
	s_lshl_b32 s74, s74, 17
	s_add_u32 s74, s74, s73
	s_add_u32 s74, s74, s76
	s_add_u32 s76, s12, s74
	s_addc_u32 s77, s13, 0
	s_bfe_u32 s74, s33, 0x20003
	s_lshl_b32 s74, s74, 15
	s_lshl_b32 s78, s75, 14
	s_add_u32 s74, s74, s78
	s_waitcnt lgkmcnt(0)
	v_readfirstlane_b32 s78, v249
	s_lshl_b32 s78, s78, 20
	s_lshl_b32 s79, s28, 17
	s_add_u32 s78, s78, s79
	s_add_u32 s78, s78, s74
	s_add_u32 s78, s44, s78
	s_addc_u32 s79, s45, 0
	s_add_u32 s74, s74, 0x100
	s_add_u32 s74, s26, s74
	s_addc_u32 s75, s27, 0
	s_lshr_b32 s71, s70, 1
	s_cmp_eq_u32 s71, 1
	s_cselect_b64 s[76:77], s[74:75], s[76:77]
	s_cmp_eq_u32 s71, 2
	s_cselect_b64 s[76:77], s[78:79], s[76:77]
	v_lshrrev_b32_e32 v250, 1, v206
	v_and_b32_e32 v249, 1, v206
	v_lshlrev_b32_e32 v250, 9, v250
	v_lshl_or_b32 v250, v249, 7, v250
	ds_read_b128 v[26:29], v191
	ds_read_b128 v[30:33], v191 offset:1024
	ds_read_b128 v[18:21], v191 offset:2048
	ds_read_b128 v[22:25], v191 offset:3072
	ds_read_b128 v[10:13], v192
	ds_read_b128 v[14:17], v192 offset:1024
	ds_read_b128 v[2:5], v192 offset:2048
	ds_read_b128 v[6:9], v192 offset:3072
	s_cmp_eq_u32 s54, s23
	s_cselect_b64 vcc, -1, 0
	s_add_i32 s23, s23, 2
	s_and_b64 s[38:39], vcc, exec
	s_cselect_b32 s38, 0, s34
	s_cselect_b32 s25, 0, s35
	s_add_u32 s38, s12, s38
	s_addc_u32 s39, s13, s25
	s_add_u32 s25, s30, s34
	s_addc_u32 s67, s31, s35
	s_and_b64 s[40:41], vcc, exec
	v_cndmask_b32_e32 v168, v197, v198, vcc
	v_cndmask_b32_e32 v202, v172, v200, vcc
	v_cndmask_b32_e32 v184, v170, v199, vcc
	s_cselect_b32 s41, s27, s67
	s_cselect_b32 s40, s26, s25
	s_mov_b32 m0, s55
	v_lshl_add_u64 v[186:187], s[36:37], 0, v[172:173]
	ds_read_b128 v[176:179], v193
	ds_read_b128 v[180:183], v193 offset:1024
	ds_read_b128 v[208:211], v193 offset:2048
	ds_read_b128 v[212:215], v193 offset:3072
	ds_read_b128 v[216:219], v193 offset:4096
	ds_read_b128 v[220:223], v193 offset:5120
	ds_read_b128 v[224:227], v193 offset:6144
	ds_read_b128 v[228:231], v193 offset:7168
	global_load_lds_dwordx4 v[186:187], off
	v_lshl_add_u64 v[186:187], s[36:37], 0, v[174:175]
	s_mov_b32 m0, s56
	s_nop 0
	global_load_lds_dwordx4 v[186:187], off
	s_waitcnt vmcnt(16)
	s_waitcnt lgkmcnt(0)
	s_barrier
	s_setprio 1
	s_waitcnt lgkmcnt(0)
	v_mfma_scale_f32_16x16x128_f8f6f4 v[158:161], v[26:33], v[176:183], 0, v188, v189 op_sel_hi:[0,0,0]
	v_mfma_scale_f32_16x16x128_f8f6f4 v[154:157], v[18:25], v[176:183], 0, v188, v189 op_sel_hi:[0,0,0]
	v_mfma_scale_f32_16x16x128_f8f6f4 v[142:145], v[26:33], v[208:215], 0, v188, v189 op_sel_hi:[0,0,0]
	v_mfma_scale_f32_16x16x128_f8f6f4 v[138:141], v[18:25], v[208:215], 0, v188, v189 op_sel_hi:[0,0,0]
	v_mfma_scale_f32_16x16x128_f8f6f4 v[126:129], v[26:33], v[216:223], 0, v188, v189 op_sel_hi:[0,0,0]
	v_mfma_scale_f32_16x16x128_f8f6f4 v[122:125], v[18:25], v[216:223], 0, v188, v189 op_sel_hi:[0,0,0]
	v_mfma_scale_f32_16x16x128_f8f6f4 v[110:113], v[26:33], v[224:231], 0, v188, v189 op_sel_hi:[0,0,0]
	v_mfma_scale_f32_16x16x128_f8f6f4 v[106:109], v[18:25], v[224:231], 0, v188, v189 op_sel_hi:[0,0,0]
	s_setprio 0
	s_setprio 1
	v_mfma_scale_f32_16x16x128_f8f6f4 v[150:153], v[10:17], v[176:183], 0, v188, v189 op_sel_hi:[0,0,0]
	v_mfma_scale_f32_16x16x128_f8f6f4 v[146:149], v[2:9], v[176:183], 0, v188, v189 op_sel_hi:[0,0,0]
	v_mfma_scale_f32_16x16x128_f8f6f4 v[134:137], v[10:17], v[208:215], 0, v188, v189 op_sel_hi:[0,0,0]
	v_mfma_scale_f32_16x16x128_f8f6f4 v[130:133], v[2:9], v[208:215], 0, v188, v189 op_sel_hi:[0,0,0]
	v_mfma_scale_f32_16x16x128_f8f6f4 v[118:121], v[10:17], v[216:223], 0, v188, v189 op_sel_hi:[0,0,0]
	v_mfma_scale_f32_16x16x128_f8f6f4 v[114:117], v[2:9], v[216:223], 0, v188, v189 op_sel_hi:[0,0,0]
	v_mfma_scale_f32_16x16x128_f8f6f4 v[102:105], v[10:17], v[224:231], 0, v188, v189 op_sel_hi:[0,0,0]
	v_mfma_scale_f32_16x16x128_f8f6f4 v[98:101], v[2:9], v[224:231], 0, v188, v189 op_sel_hi:[0,0,0]
	s_setprio 0
	s_barrier
	s_mov_b32 m0, s57
	v_lshl_add_u64 v[176:177], s[40:41], 0, v[166:167]
	v_lshl_add_u64 v[178:179], s[40:41], 0, v[164:165]
	s_add_u32 s40, s40, s10
	ds_read_b128 v[208:211], v193 offset:16384
	ds_read_b128 v[212:215], v193 offset:17408
	ds_read_b128 v[216:219], v193 offset:18432
	ds_read_b128 v[220:223], v193 offset:19456
	ds_read_b128 v[224:227], v193 offset:20480
	ds_read_b128 v[228:231], v193 offset:21504
	ds_read_b128 v[232:235], v193 offset:22528
	ds_read_b128 v[236:239], v193 offset:23552
	global_load_lds_dwordx4 v[176:177], off
	s_mov_b32 m0, s58
	s_addc_u32 s41, s41, s11
	global_load_lds_dwordx4 v[178:179], off
	v_lshl_add_u64 v[180:181], s[40:41], 0, v[166:167]
	s_mov_b32 m0, s59
	v_lshl_add_u64 v[182:183], s[40:41], 0, v[164:165]
	global_load_lds_dwordx4 v[180:181], off
	s_mov_b32 m0, s60
	v_mov_b32_e32 v185, v169
	global_load_lds_dwordx4 v[182:183], off
	s_mov_b32 m0, s29
	v_lshl_add_u64 v[186:187], s[38:39], 0, v[168:169]
	global_load_lds_dwordx4 v168, s[38:39]
	s_mov_b32 m0, s46
	s_nop 0
	global_load_lds_dwordx4 v184, s[38:39]
	global_load_dword v251, v250, s[76:77]
	s_waitcnt vmcnt(17)
	s_waitcnt lgkmcnt(0)
	v_lshl_add_u64 v[184:185], s[38:39], 0, v[184:185]
	s_barrier
	s_setprio 1
	s_waitcnt lgkmcnt(0)
	v_mfma_scale_f32_16x16x128_f8f6f4 v[94:97], v[26:33], v[208:215], 0, v188, v189 op_sel_hi:[0,0,0]
	v_mfma_scale_f32_16x16x128_f8f6f4 v[90:93], v[18:25], v[208:215], 0, v188, v189 op_sel_hi:[0,0,0]
	v_mfma_scale_f32_16x16x128_f8f6f4 v[78:81], v[26:33], v[216:223], 0, v188, v189 op_sel_hi:[0,0,0]
	v_mfma_scale_f32_16x16x128_f8f6f4 v[74:77], v[18:25], v[216:223], 0, v188, v189 op_sel_hi:[0,0,0]
	v_mfma_scale_f32_16x16x128_f8f6f4 v[62:65], v[26:33], v[224:231], 0, v188, v189 op_sel_hi:[0,0,0]
	v_mfma_scale_f32_16x16x128_f8f6f4 v[58:61], v[18:25], v[224:231], 0, v188, v189 op_sel_hi:[0,0,0]
	v_mfma_scale_f32_16x16x128_f8f6f4 v[46:49], v[26:33], v[232:239], 0, v188, v189 op_sel_hi:[0,0,0]
	v_mfma_scale_f32_16x16x128_f8f6f4 v[42:45], v[18:25], v[232:239], 0, v188, v189 op_sel_hi:[0,0,0]
	s_setprio 0
	s_setprio 1
	v_mfma_scale_f32_16x16x128_f8f6f4 v[86:89], v[10:17], v[208:215], 0, v188, v189 op_sel_hi:[0,0,0]
	v_mfma_scale_f32_16x16x128_f8f6f4 v[82:85], v[2:9], v[208:215], 0, v188, v189 op_sel_hi:[0,0,0]
	v_mfma_scale_f32_16x16x128_f8f6f4 v[70:73], v[10:17], v[216:223], 0, v188, v189 op_sel_hi:[0,0,0]
	v_mfma_scale_f32_16x16x128_f8f6f4 v[66:69], v[2:9], v[216:223], 0, v188, v189 op_sel_hi:[0,0,0]
	v_mfma_scale_f32_16x16x128_f8f6f4 v[54:57], v[10:17], v[224:231], 0, v188, v189 op_sel_hi:[0,0,0]
	v_mfma_scale_f32_16x16x128_f8f6f4 v[50:53], v[2:9], v[224:231], 0, v188, v189 op_sel_hi:[0,0,0]
	v_mfma_scale_f32_16x16x128_f8f6f4 v[38:41], v[10:17], v[232:239], 0, v188, v189 op_sel_hi:[0,0,0]
	v_mfma_scale_f32_16x16x128_f8f6f4 v[34:37], v[2:9], v[232:239], 0, v188, v189 op_sel_hi:[0,0,0]
	s_setprio 0
	s_barrier
	ds_read_b128 v[26:29], v194
	ds_read_b128 v[30:33], v194 offset:1024
	ds_read_b128 v[18:21], v194 offset:2048
	ds_read_b128 v[22:25], v194 offset:3072
	ds_read_b128 v[10:13], v195
	ds_read_b128 v[14:17], v195 offset:1024
	ds_read_b128 v[2:5], v195 offset:2048
	ds_read_b128 v[6:9], v195 offset:3072
	s_mov_b32 m0, s47
	ds_read_b128 v[208:211], v193 offset:32768
	ds_read_b128 v[212:215], v193 offset:33792
	ds_read_b128 v[216:219], v193 offset:34816
	ds_read_b128 v[220:223], v193 offset:35840
	ds_read_b128 v[224:227], v193 offset:36864
	ds_read_b128 v[228:231], v193 offset:37888
	ds_read_b128 v[232:235], v193 offset:38912
	ds_read_b128 v[236:239], v193 offset:39936
	v_cndmask_b32_e32 v168, v174, v201, vcc
	global_load_lds_dwordx4 v202, s[38:39]
	s_mov_b32 m0, s48
	s_nop 0
	global_load_lds_dwordx4 v168, s[38:39]
	s_waitcnt vmcnt(9)
	s_waitcnt lgkmcnt(0)
	s_barrier
	s_setprio 1
	s_waitcnt lgkmcnt(0)
	v_mfma_scale_f32_16x16x128_f8f6f4 v[158:161], v[26:33], v[208:215], v[158:161], v188, v189 op_sel_hi:[0,0,0]
	v_mfma_scale_f32_16x16x128_f8f6f4 v[154:157], v[18:25], v[208:215], v[154:157], v188, v189 op_sel_hi:[0,0,0]
	v_mfma_scale_f32_16x16x128_f8f6f4 v[142:145], v[26:33], v[216:223], v[142:145], v188, v189 op_sel_hi:[0,0,0]
	v_mfma_scale_f32_16x16x128_f8f6f4 v[138:141], v[18:25], v[216:223], v[138:141], v188, v189 op_sel_hi:[0,0,0]
	v_mfma_scale_f32_16x16x128_f8f6f4 v[126:129], v[26:33], v[224:231], v[126:129], v188, v189 op_sel_hi:[0,0,0]
	v_mfma_scale_f32_16x16x128_f8f6f4 v[122:125], v[18:25], v[224:231], v[122:125], v188, v189 op_sel_hi:[0,0,0]
	v_mfma_scale_f32_16x16x128_f8f6f4 v[110:113], v[26:33], v[232:239], v[110:113], v188, v189 op_sel_hi:[0,0,0]
	v_mfma_scale_f32_16x16x128_f8f6f4 v[106:109], v[18:25], v[232:239], v[106:109], v188, v189 op_sel_hi:[0,0,0]
	s_setprio 0
	s_setprio 1
	v_mfma_scale_f32_16x16x128_f8f6f4 v[150:153], v[10:17], v[208:215], v[150:153], v188, v189 op_sel_hi:[0,0,0]
	v_mfma_scale_f32_16x16x128_f8f6f4 v[146:149], v[2:9], v[208:215], v[146:149], v188, v189 op_sel_hi:[0,0,0]
	v_mfma_scale_f32_16x16x128_f8f6f4 v[134:137], v[10:17], v[216:223], v[134:137], v188, v189 op_sel_hi:[0,0,0]
	v_mfma_scale_f32_16x16x128_f8f6f4 v[130:133], v[2:9], v[216:223], v[130:133], v188, v189 op_sel_hi:[0,0,0]
	v_mfma_scale_f32_16x16x128_f8f6f4 v[118:121], v[10:17], v[224:231], v[118:121], v188, v189 op_sel_hi:[0,0,0]
	v_mfma_scale_f32_16x16x128_f8f6f4 v[114:117], v[2:9], v[224:231], v[114:117], v188, v189 op_sel_hi:[0,0,0]
	v_mfma_scale_f32_16x16x128_f8f6f4 v[102:105], v[10:17], v[232:239], v[102:105], v188, v189 op_sel_hi:[0,0,0]
	v_mfma_scale_f32_16x16x128_f8f6f4 v[98:101], v[2:9], v[232:239], v[98:101], v188, v189 op_sel_hi:[0,0,0]
	s_setprio 0
	s_barrier
	s_mov_b32 m0, s61
	v_lshl_add_u64 v[176:177], v[176:177], 0, s[18:19]
	ds_read_b128 v[208:211], v193 offset:49152
	ds_read_b128 v[212:215], v193 offset:50176
	ds_read_b128 v[216:219], v193 offset:51200
	ds_read_b128 v[220:223], v193 offset:52224
	ds_read_b128 v[224:227], v193 offset:53248
	ds_read_b128 v[228:231], v193 offset:54272
	ds_read_b128 v[232:235], v193 offset:55296
	ds_read_b128 v[236:239], v193 offset:56320
	global_load_lds_dwordx4 v[176:177], off
	v_lshl_add_u64 v[176:177], v[178:179], 0, s[18:19]
	s_mov_b32 m0, s62
	s_nop 0
	global_load_lds_dwordx4 v[176:177], off
	v_lshl_add_u64 v[176:177], v[180:181], 0, s[18:19]
	s_mov_b32 m0, s63
	s_nop 0
	global_load_lds_dwordx4 v[176:177], off
	v_lshl_add_u64 v[176:177], v[182:183], 0, s[18:19]
	s_add_i32 m0, s63, 0x2000
	s_nop 0
	global_load_lds_dwordx4 v[176:177], off
	v_lshl_add_u64 v[176:177], v[186:187], 0, s[18:19]
	s_mov_b32 m0, s50
	s_nop 0
	global_load_lds_dwordx4 v[176:177], off
	v_lshl_add_u64 v[176:177], v[184:185], 0, s[18:19]
	s_mov_b32 m0, s51
	s_nop 0
	global_load_lds_dwordx4 v[176:177], off
	s_waitcnt vmcnt(9)
	s_waitcnt lgkmcnt(0)
	s_barrier
	s_setprio 1
	s_waitcnt lgkmcnt(0)
	v_mfma_scale_f32_16x16x128_f8f6f4 v[94:97], v[26:33], v[208:215], v[94:97], v188, v189 op_sel_hi:[0,0,0]
	v_mfma_scale_f32_16x16x128_f8f6f4 v[90:93], v[18:25], v[208:215], v[90:93], v188, v189 op_sel_hi:[0,0,0]
	v_mfma_scale_f32_16x16x128_f8f6f4 v[78:81], v[26:33], v[216:223], v[78:81], v188, v189 op_sel_hi:[0,0,0]
	v_mfma_scale_f32_16x16x128_f8f6f4 v[74:77], v[18:25], v[216:223], v[74:77], v188, v189 op_sel_hi:[0,0,0]
	v_mfma_scale_f32_16x16x128_f8f6f4 v[62:65], v[26:33], v[224:231], v[62:65], v188, v189 op_sel_hi:[0,0,0]
	v_mfma_scale_f32_16x16x128_f8f6f4 v[58:61], v[18:25], v[224:231], v[58:61], v188, v189 op_sel_hi:[0,0,0]
	v_mfma_scale_f32_16x16x128_f8f6f4 v[46:49], v[26:33], v[232:239], v[46:49], v188, v189 op_sel_hi:[0,0,0]
	v_mfma_scale_f32_16x16x128_f8f6f4 v[42:45], v[18:25], v[232:239], v[42:45], v188, v189 op_sel_hi:[0,0,0]
	s_setprio 0
	s_setprio 1
	v_mfma_scale_f32_16x16x128_f8f6f4 v[86:89], v[10:17], v[208:215], v[86:89], v188, v189 op_sel_hi:[0,0,0]
	v_mfma_scale_f32_16x16x128_f8f6f4 v[82:85], v[2:9], v[208:215], v[82:85], v188, v189 op_sel_hi:[0,0,0]
	v_mfma_scale_f32_16x16x128_f8f6f4 v[70:73], v[10:17], v[216:223], v[70:73], v188, v189 op_sel_hi:[0,0,0]
	v_mfma_scale_f32_16x16x128_f8f6f4 v[66:69], v[2:9], v[216:223], v[66:69], v188, v189 op_sel_hi:[0,0,0]
	v_mfma_scale_f32_16x16x128_f8f6f4 v[54:57], v[10:17], v[224:231], v[54:57], v188, v189 op_sel_hi:[0,0,0]
	v_mfma_scale_f32_16x16x128_f8f6f4 v[50:53], v[2:9], v[224:231], v[50:53], v188, v189 op_sel_hi:[0,0,0]
	v_mfma_scale_f32_16x16x128_f8f6f4 v[38:41], v[10:17], v[232:239], v[38:41], v188, v189 op_sel_hi:[0,0,0]
	v_mfma_scale_f32_16x16x128_f8f6f4 v[34:37], v[2:9], v[232:239], v[34:37], v188, v189 op_sel_hi:[0,0,0]
	s_setprio 0
	s_barrier
	s_add_u32 s34, s34, 0x100
	s_addc_u32 s35, s35, 0
	s_add_u32 s36, s36, 0x100
	s_addc_u32 s37, s37, 0
	s_cmp_ge_i32 s23, s49
	s_cbranch_scc1 .LBB0_1444
	s_branch .LBB0_1443
